# speedup vs baseline: 1.1570x; 1.0023x over previous
_Z8attn_fwdPKfPKiPf:
	s_load_dwordx4 s[4:7], s[0:1], 0x0
	s_load_dwordx2 s[12:13], s[0:1], 0x10
	v_and_b32_e32 v235, 63, v0
	v_lshrrev_b32_e32 v236, 4, v0
	v_and_b32_e32 v237, 15, v0
	v_readfirstlane_b32 s17, v0
	s_nop 3
	s_lshr_b32 s17, s17, 6
	v_mul_u32_u24_e32 v229, 0x3000, v236
	v_lshl_add_u32 v229, v237, 4, v229
	v_lshlrev_b32_e32 v230, 2, v235
	v_and_b32_e32 v238, 31, v0
	v_bfe_u32 v234, v0, 5, 1
	v_lshrrev_b32_e32 v231, 4, v235
	v_mul_u32_u24_e32 v243, 0x3000, v231
	v_lshl_add_u32 v243, v237, 4, v243
	s_and_b32 s33, s2, 7
	s_lshr_b32 s31, s2, 3
	s_and_b32 s39, s31, 3
	s_lshr_b32 s40, s31, 3
	s_lshr_b32 s41, s31, 2
	s_and_b32 s41, s41, 1
	s_lshl_b32 s33, s33, 1
	s_add_u32 s41, s41, s33
	s_mul_i32 s16, s40, 0x1800000
	s_lshl_b32 s31, s41, 8
	s_add_u32 s16, s16, s31
	s_add_u32 s18, s16, 4096
	s_lshr_b32 s31, s17, 1
	s_lshl_b32 s31, s31, 4
	s_and_b32 s33, s17, 1
	s_lshl_b32 s33, s33, 2
	s_add_u32 s31, s31, s33
	s_mul_i32 s31, s31, 0x3000
	s_add_u32 s19, s16, 8192
	s_add_u32 s19, s19, s31
	s_lshl_b32 s22, s40, 13
	s_lshl_b32 s31, s39, 8
	s_lshl_b32 s33, s17, 5
	s_add_u32 s31, s31, s33
	s_mul_i32 s29, s31, 0x3000
	s_add_u32 s29, s29, s16
	s_lshl_b32 s33, s40, 11
	s_add_u32 s31, s31, s33
	s_lshl_b32 s30, s31, 12
	s_lshl_b32 s31, s41, 8
	s_add_u32 s30, s30, s31
	s_mov_b32 s37, 0x46800000
	s_mov_b32 s38, 0xbf800000
	s_mov_b32 s34, 0x46800000
	s_mov_b32 s35, 0xc6616bcd
	s_mov_b32 s36, 0x3e38aa3b
	s_mov_b32 s23, 0
	s_mov_b32 s27, 0
	s_mov_b32 s42, 0
	s_waitcnt lgkmcnt(0)
	s_mov_b32 s8, s6
	s_and_b32 s9, s7, 0xffff
	s_mov_b32 s10, 0x7fffffff
	s_mov_b32 s11, 0x20000
	s_and_b32 s5, s5, 0xffff
	s_mov_b32 s6, 0x7fffffff
	s_mov_b32 s7, 0x20000
	s_and_b32 s13, s13, 0xffff
	s_mov_b32 s14, 0x7fffffff
	s_mov_b32 s15, 0x20000
	s_add_u32 s31, s18, 0x0
	buffer_load_dwordx4 v[64:67], v229, s[4:7], s31 offen
	s_add_u32 s31, s18, 0x60000
	buffer_load_dwordx4 v[68:71], v229, s[4:7], s31 offen
	buffer_load_dword v224, v230, s[8:11], s22 offen
	s_add_u32 s31, s18, 0xc0000
	buffer_load_dwordx4 v[72:75], v229, s[4:7], s31 offen
	s_add_u32 s31, s18, 0x120000
	buffer_load_dwordx4 v[76:79], v229, s[4:7], s31 offen
	s_add_u32 s31, s19, 0x0
	buffer_load_dword v80, v230, s[4:7], s31 offen
	s_add_u32 s31, s19, 0x3000
	buffer_load_dword v81, v230, s[4:7], s31 offen
	s_add_u32 s31, s19, 0x6000
	buffer_load_dword v82, v230, s[4:7], s31 offen
	s_add_u32 s31, s19, 0x9000
	buffer_load_dword v83, v230, s[4:7], s31 offen
	s_add_u32 s31, s19, 0x18000
	buffer_load_dword v84, v230, s[4:7], s31 offen
	s_add_u32 s31, s19, 0x1b000
	buffer_load_dword v85, v230, s[4:7], s31 offen
	s_add_u32 s31, s19, 0x1e000
	buffer_load_dword v86, v230, s[4:7], s31 offen
	s_add_u32 s31, s19, 0x21000
	buffer_load_dword v87, v230, s[4:7], s31 offen
	s_add_u32 s31, s29, 0x0
	buffer_load_dwordx4 v[0:3], v243, s[4:7], s31 offen nt
	s_add_u32 s31, s29, 0xc000
	buffer_load_dwordx4 v[4:7], v243, s[4:7], s31 offen nt
	s_add_u32 s31, s29, 0x18000
	buffer_load_dwordx4 v[8:11], v243, s[4:7], s31 offen nt
	s_add_u32 s31, s29, 0x24000
	buffer_load_dwordx4 v[12:15], v243, s[4:7], s31 offen nt
	s_add_u32 s31, s29, 0x30000
	buffer_load_dwordx4 v[16:19], v243, s[4:7], s31 offen nt
	s_add_u32 s31, s29, 0x3c000
	buffer_load_dwordx4 v[20:23], v243, s[4:7], s31 offen nt
	s_add_u32 s31, s29, 0x48000
	buffer_load_dwordx4 v[24:27], v243, s[4:7], s31 offen nt
	s_add_u32 s31, s29, 0x54000
	buffer_load_dwordx4 v[28:31], v243, s[4:7], s31 offen nt
	v_mul_u32_u24_e32 v227, 144, v236
	v_lshl_add_u32 v227, v237, 3, v227
	v_mov_b32_e32 v236, v234
	v_mul_u32_u24_e32 v225, 144, v238
	v_lshl_add_u32 v225, v236, 4, v225
	v_add_u32_e32 v226, 36864, v225
	v_lshlrev_b32_e32 v234, 2, v236
	v_mul_u32_u24_e32 v228, 144, v235
	s_lshl_b32 s31, s17, 4
	s_add_u32 s31, s31, 36864
	v_add_u32_e32 v228, s31, v228
	s_mul_i32 s32, s17, 8704
	s_add_u32 s32, s32, 73728
	v_mul_u32_u24_e32 v239, 144, v231
	v_lshl_add_u32 v239, v237, 3, v239
	v_add_u32_e32 v239, s32, v239
	v_add_u32_e32 v240, s32, v225
	v_mul_u32_u24_e32 v241, 272, v238
	v_lshl_add_u32 v241, v236, 4, v241
	v_add_u32_e32 v241, s32, v241
	v_mul_u32_u24_e32 v242, 272, v231
	v_lshl_add_u32 v242, v237, 4, v242
	v_add_u32_e32 v242, s32, v242
	v_lshlrev_b32_e32 v244, 12, v231
	v_lshl_add_u32 v244, v237, 4, v244
	s_waitcnt vmcnt(8)
	v_cvt_pk_f16_f32 v64, v64, v65
	v_cvt_pk_f16_f32 v65, v66, v67
	ds_write_b64 v227, v[64:65] offset:0
	v_cvt_pk_f16_f32 v68, v68, v69
	v_cvt_pk_f16_f32 v69, v70, v71
	ds_write_b64 v227, v[68:69] offset:4608
	v_cvt_pk_f16_f32 v72, v72, v73
	v_cvt_pk_f16_f32 v73, v74, v75
	ds_write_b64 v227, v[72:73] offset:9216
	v_cvt_pk_f16_f32 v76, v76, v77
	v_cvt_pk_f16_f32 v77, v78, v79
	ds_write_b64 v227, v[76:77] offset:13824
	v_cvt_pk_f16_f32 v80, v80, v81
	v_cvt_pk_f16_f32 v81, v82, v83
	v_cvt_pk_f16_f32 v82, v84, v85
	v_cvt_pk_f16_f32 v83, v86, v87
	ds_write_b128 v228, v[80:83] offset:0
	s_add_u32 s31, s18, 0x180000
	buffer_load_dwordx4 v[208:211], v229, s[4:7], s31 offen
	s_add_u32 s31, s18, 0x1e0000
	buffer_load_dwordx4 v[212:215], v229, s[4:7], s31 offen
	s_add_u32 s31, s19, 0xc0000
	buffer_load_dword v216, v230, s[4:7], s31 offen
	s_add_u32 s31, s19, 0xc3000
	buffer_load_dword v217, v230, s[4:7], s31 offen
	s_add_u32 s31, s19, 0xc6000
	buffer_load_dword v218, v230, s[4:7], s31 offen
	s_add_u32 s31, s19, 0xc9000
	buffer_load_dword v219, v230, s[4:7], s31 offen
	s_add_u32 s31, s19, 0xd8000
	buffer_load_dword v220, v230, s[4:7], s31 offen
	s_add_u32 s31, s19, 0xdb000
	buffer_load_dword v221, v230, s[4:7], s31 offen
	s_add_u32 s31, s19, 0xde000
	buffer_load_dword v222, v230, s[4:7], s31 offen
	s_add_u32 s31, s19, 0xe1000
	buffer_load_dword v223, v230, s[4:7], s31 offen
	s_waitcnt vmcnt(10)
	v_mul_f32_e32 v0, s36, v0
	v_mul_f32_e32 v1, s36, v1
	v_mul_f32_e32 v2, s36, v2
	v_mul_f32_e32 v3, s36, v3
	v_cvt_pk_f16_f32 v0, v0, v1
	v_cvt_pk_f16_f32 v1, v2, v3
	ds_write_b64 v239, v[0:1] offset:0
	v_mul_f32_e32 v4, s36, v4
	v_mul_f32_e32 v5, s36, v5
	v_mul_f32_e32 v6, s36, v6
	v_mul_f32_e32 v7, s36, v7
	v_cvt_pk_f16_f32 v4, v4, v5
	v_cvt_pk_f16_f32 v5, v6, v7
	ds_write_b64 v239, v[4:5] offset:576
	v_mul_f32_e32 v8, s36, v8
	v_mul_f32_e32 v9, s36, v9
	v_mul_f32_e32 v10, s36, v10
	v_mul_f32_e32 v11, s36, v11
	v_cvt_pk_f16_f32 v8, v8, v9
	v_cvt_pk_f16_f32 v9, v10, v11
	ds_write_b64 v239, v[8:9] offset:1152
	v_mul_f32_e32 v12, s36, v12
	v_mul_f32_e32 v13, s36, v13
	v_mul_f32_e32 v14, s36, v14
	v_mul_f32_e32 v15, s36, v15
	v_cvt_pk_f16_f32 v12, v12, v13
	v_cvt_pk_f16_f32 v13, v14, v15
	ds_write_b64 v239, v[12:13] offset:1728
	v_mul_f32_e32 v16, s36, v16
	v_mul_f32_e32 v17, s36, v17
	v_mul_f32_e32 v18, s36, v18
	v_mul_f32_e32 v19, s36, v19
	v_cvt_pk_f16_f32 v16, v16, v17
	v_cvt_pk_f16_f32 v17, v18, v19
	ds_write_b64 v239, v[16:17] offset:2304
	v_mul_f32_e32 v20, s36, v20
	v_mul_f32_e32 v21, s36, v21
	v_mul_f32_e32 v22, s36, v22
	v_mul_f32_e32 v23, s36, v23
	v_cvt_pk_f16_f32 v20, v20, v21
	v_cvt_pk_f16_f32 v21, v22, v23
	ds_write_b64 v239, v[20:21] offset:2880
	v_mul_f32_e32 v24, s36, v24
	v_mul_f32_e32 v25, s36, v25
	v_mul_f32_e32 v26, s36, v26
	v_mul_f32_e32 v27, s36, v27
	v_cvt_pk_f16_f32 v24, v24, v25
	v_cvt_pk_f16_f32 v25, v26, v27
	ds_write_b64 v239, v[24:25] offset:3456
	v_mul_f32_e32 v28, s36, v28
	v_mul_f32_e32 v29, s36, v29
	v_mul_f32_e32 v30, s36, v30
	v_mul_f32_e32 v31, s36, v31
	v_cvt_pk_f16_f32 v28, v28, v29
	v_cvt_pk_f16_f32 v29, v30, v31
	ds_write_b64 v239, v[28:29] offset:4032
	s_waitcnt lgkmcnt(0)
	ds_read_b128 v[128:131], v240 offset:0
	ds_read_b128 v[132:135], v240 offset:32
	ds_read_b128 v[136:139], v240 offset:64
	ds_read_b128 v[140:143], v240 offset:96
	s_waitcnt lgkmcnt(0)
	s_barrier
	ds_read_b128 v[176:179], v225 offset:0
	ds_read_b128 v[180:183], v225 offset:32
	ds_read_b128 v[184:187], v225 offset:64
	ds_read_b128 v[188:191], v225 offset:96
	ds_read_b128 v[192:195], v225 offset:4608
	ds_read_b128 v[196:199], v225 offset:4640
	ds_read_b128 v[200:203], v225 offset:4672
	ds_read_b128 v[204:207], v225 offset:4704
	s_waitcnt lgkmcnt(0)
	v_cmp_ne_u32_e64 s[20:21], 0, v224
	v_mfma_f32_32x32x16_f16 v[64:79], v[176:179], v[128:131], 0
	v_mfma_f32_32x32x16_f16 v[64:79], v[180:183], v[132:135], v[64:79]
	v_mfma_f32_32x32x16_f16 v[64:79], v[184:187], v[136:139], v[64:79]
	v_mfma_f32_32x32x16_f16 v[64:79], v[188:191], v[140:143], v[64:79]
	v_mfma_f32_32x32x16_f16 v[80:95], v[192:195], v[128:131], 0
	v_mfma_f32_32x32x16_f16 v[80:95], v[196:199], v[132:135], v[80:95]
	v_mfma_f32_32x32x16_f16 v[80:95], v[200:203], v[136:139], v[80:95]
	v_mfma_f32_32x32x16_f16 v[80:95], v[204:207], v[140:143], v[80:95]
	s_nop 15
	s_nop 3
	s_cmp_eq_u64 s[20:21], -1
	s_cbranch_scc1 .Lpro_nomask_A
	v_lshrrev_b32_e64 v235, v234, s20
	v_bfe_u32 v236, v235, 0, 1
	v_cvt_f32_u32_e32 v236, v236
	v_sub_f32_e32 v236, 1.0, v236
	v_fmac_f32_e32 v64, s35, v236
	v_bfe_u32 v236, v235, 1, 1
	v_cvt_f32_u32_e32 v236, v236
	v_sub_f32_e32 v236, 1.0, v236
	v_fmac_f32_e32 v65, s35, v236
	v_bfe_u32 v236, v235, 2, 1
	v_cvt_f32_u32_e32 v236, v236
	v_sub_f32_e32 v236, 1.0, v236
	v_fmac_f32_e32 v66, s35, v236
	v_bfe_u32 v236, v235, 3, 1
	v_cvt_f32_u32_e32 v236, v236
	v_sub_f32_e32 v236, 1.0, v236
	v_fmac_f32_e32 v67, s35, v236
	v_bfe_u32 v236, v235, 8, 1
	v_cvt_f32_u32_e32 v236, v236
	v_sub_f32_e32 v236, 1.0, v236
	v_fmac_f32_e32 v68, s35, v236
	v_bfe_u32 v236, v235, 9, 1
	v_cvt_f32_u32_e32 v236, v236
	v_sub_f32_e32 v236, 1.0, v236
	v_fmac_f32_e32 v69, s35, v236
	v_bfe_u32 v236, v235, 10, 1
	v_cvt_f32_u32_e32 v236, v236
	v_sub_f32_e32 v236, 1.0, v236
	v_fmac_f32_e32 v70, s35, v236
	v_bfe_u32 v236, v235, 11, 1
	v_cvt_f32_u32_e32 v236, v236
	v_sub_f32_e32 v236, 1.0, v236
	v_fmac_f32_e32 v71, s35, v236
	v_bfe_u32 v236, v235, 16, 1
	v_cvt_f32_u32_e32 v236, v236
	v_sub_f32_e32 v236, 1.0, v236
	v_fmac_f32_e32 v72, s35, v236
	v_bfe_u32 v236, v235, 17, 1
	v_cvt_f32_u32_e32 v236, v236
	v_sub_f32_e32 v236, 1.0, v236
	v_fmac_f32_e32 v73, s35, v236
	v_bfe_u32 v236, v235, 18, 1
	v_cvt_f32_u32_e32 v236, v236
	v_sub_f32_e32 v236, 1.0, v236
	v_fmac_f32_e32 v74, s35, v236
	v_bfe_u32 v236, v235, 19, 1
	v_cvt_f32_u32_e32 v236, v236
	v_sub_f32_e32 v236, 1.0, v236
	v_fmac_f32_e32 v75, s35, v236
	v_bfe_u32 v236, v235, 24, 1
	v_cvt_f32_u32_e32 v236, v236
	v_sub_f32_e32 v236, 1.0, v236
	v_fmac_f32_e32 v76, s35, v236
	v_bfe_u32 v236, v235, 25, 1
	v_cvt_f32_u32_e32 v236, v236
	v_sub_f32_e32 v236, 1.0, v236
	v_fmac_f32_e32 v77, s35, v236
	v_bfe_u32 v236, v235, 26, 1
	v_cvt_f32_u32_e32 v236, v236
	v_sub_f32_e32 v236, 1.0, v236
	v_fmac_f32_e32 v78, s35, v236
	v_bfe_u32 v236, v235, 27, 1
	v_cvt_f32_u32_e32 v236, v236
	v_sub_f32_e32 v236, 1.0, v236
	v_fmac_f32_e32 v79, s35, v236
	v_lshrrev_b32_e64 v235, v234, s21
	v_bfe_u32 v236, v235, 0, 1
	v_cvt_f32_u32_e32 v236, v236
	v_sub_f32_e32 v236, 1.0, v236
	v_fmac_f32_e32 v80, s35, v236
	v_bfe_u32 v236, v235, 1, 1
	v_cvt_f32_u32_e32 v236, v236
	v_sub_f32_e32 v236, 1.0, v236
	v_fmac_f32_e32 v81, s35, v236
	v_bfe_u32 v236, v235, 2, 1
	v_cvt_f32_u32_e32 v236, v236
	v_sub_f32_e32 v236, 1.0, v236
	v_fmac_f32_e32 v82, s35, v236
	v_bfe_u32 v236, v235, 3, 1
	v_cvt_f32_u32_e32 v236, v236
	v_sub_f32_e32 v236, 1.0, v236
	v_fmac_f32_e32 v83, s35, v236
	v_bfe_u32 v236, v235, 8, 1
	v_cvt_f32_u32_e32 v236, v236
	v_sub_f32_e32 v236, 1.0, v236
	v_fmac_f32_e32 v84, s35, v236
	v_bfe_u32 v236, v235, 9, 1
	v_cvt_f32_u32_e32 v236, v236
	v_sub_f32_e32 v236, 1.0, v236
	v_fmac_f32_e32 v85, s35, v236
	v_bfe_u32 v236, v235, 10, 1
	v_cvt_f32_u32_e32 v236, v236
	v_sub_f32_e32 v236, 1.0, v236
	v_fmac_f32_e32 v86, s35, v236
	v_bfe_u32 v236, v235, 11, 1
	v_cvt_f32_u32_e32 v236, v236
	v_sub_f32_e32 v236, 1.0, v236
	v_fmac_f32_e32 v87, s35, v236
	v_bfe_u32 v236, v235, 16, 1
	v_cvt_f32_u32_e32 v236, v236
	v_sub_f32_e32 v236, 1.0, v236
	v_fmac_f32_e32 v88, s35, v236
	v_bfe_u32 v236, v235, 17, 1
	v_cvt_f32_u32_e32 v236, v236
	v_sub_f32_e32 v236, 1.0, v236
	v_fmac_f32_e32 v89, s35, v236
	v_bfe_u32 v236, v235, 18, 1
	v_cvt_f32_u32_e32 v236, v236
	v_sub_f32_e32 v236, 1.0, v236
	v_fmac_f32_e32 v90, s35, v236
	v_bfe_u32 v236, v235, 19, 1
	v_cvt_f32_u32_e32 v236, v236
	v_sub_f32_e32 v236, 1.0, v236
	v_fmac_f32_e32 v91, s35, v236
	v_bfe_u32 v236, v235, 24, 1
	v_cvt_f32_u32_e32 v236, v236
	v_sub_f32_e32 v236, 1.0, v236
	v_fmac_f32_e32 v92, s35, v236
	v_bfe_u32 v236, v235, 25, 1
	v_cvt_f32_u32_e32 v236, v236
	v_sub_f32_e32 v236, 1.0, v236
	v_fmac_f32_e32 v93, s35, v236
	v_bfe_u32 v236, v235, 26, 1
	v_cvt_f32_u32_e32 v236, v236
	v_sub_f32_e32 v236, 1.0, v236
	v_fmac_f32_e32 v94, s35, v236
	v_bfe_u32 v236, v235, 27, 1
	v_cvt_f32_u32_e32 v236, v236
	v_sub_f32_e32 v236, 1.0, v236
	v_fmac_f32_e32 v95, s35, v236
